# v15 + counted-wait software pipelining of the adaLN GEMV loop: two 8-row load sets (16 dwordx4 loads per thread) in flight instead of a drained 8-load batch per iteration
# speedup vs baseline: 1.0056x; 1.0056x over previous
; __device__ __forceinline__ void ada_phase(LAS float* sm, int bid, int G, const float* c, const float* ada_w, const float* ada_b, float* ada) {
;     ...
;     for (int j = bid; j < 192; j += G) {
;         const int l = j / 96, cb = j - l * 96;
;         const float* w = ada_w + (size_t)l * D * 12288 + (size_t)(kg * 128) * 12288 + cb * 128 + c4 * 4;
;         float4 a = make_float4(0.f, 0.f, 0.f, 0.f);
; #pragma unroll 8
;         for (int k = 0; k < 128; ++k) { const float4 wv = *(const float4*)(w + (size_t)k * 12288); const float s = cs[kg * 128 + k]; a.x += s * wv.x; a.y += s * wv.y; a.z += s * wv.z; a.w += s * wv.w; }
.Lada_pre:
	s_mov_b64 s[22:23], 0xc000
	s_mov_b64 s[24:25], 0x18000
	s_mov_b64 s[26:27], 0x24000
	s_mov_b64 s[28:29], 0x30000
	s_mov_b64 s[30:31], 0x3c000
	s_mov_b64 s[32:33], 0x48000
	s_mov_b64 s[34:35], 0x54000
	s_mov_b32 s36, 0
	v_lshl_add_u64 v[140:141], v[10:11], 0, s[4:5]
	global_load_dwordx4 v[60:63], v[140:141], off nt
	v_lshl_add_u64 v[142:143], v[140:141], 0, s[22:23]
	global_load_dwordx4 v[64:67], v[142:143], off nt
	v_lshl_add_u64 v[142:143], v[140:141], 0, s[24:25]
	global_load_dwordx4 v[68:71], v[142:143], off nt
	v_lshl_add_u64 v[142:143], v[140:141], 0, s[26:27]
	global_load_dwordx4 v[72:75], v[142:143], off nt
	v_lshl_add_u64 v[142:143], v[140:141], 0, s[28:29]
	global_load_dwordx4 v[76:79], v[142:143], off nt
	v_lshl_add_u64 v[142:143], v[140:141], 0, s[30:31]
	global_load_dwordx4 v[80:83], v[142:143], off nt
	v_lshl_add_u64 v[142:143], v[140:141], 0, s[32:33]
	global_load_dwordx4 v[84:87], v[142:143], off nt
	v_lshl_add_u64 v[142:143], v[140:141], 0, s[34:35]
	global_load_dwordx4 v[88:91], v[142:143], off nt
	s_add_u32 s4, s4, 0x60000
	s_addc_u32 s5, s5, 0
	ds_read_b128 v[124:127], v13
	ds_read_b128 v[128:131], v13 offset:16
	v_add_u32_e32 v13, 32, v13
.Lada_loop:
	v_lshl_add_u64 v[140:141], v[10:11], 0, s[4:5]
	global_load_dwordx4 v[92:95], v[140:141], off nt
	v_lshl_add_u64 v[142:143], v[140:141], 0, s[22:23]
	global_load_dwordx4 v[96:99], v[142:143], off nt
	v_lshl_add_u64 v[142:143], v[140:141], 0, s[24:25]
	global_load_dwordx4 v[100:103], v[142:143], off nt
	v_lshl_add_u64 v[142:143], v[140:141], 0, s[26:27]
	global_load_dwordx4 v[104:107], v[142:143], off nt
	v_lshl_add_u64 v[142:143], v[140:141], 0, s[28:29]
	global_load_dwordx4 v[108:111], v[142:143], off nt
	v_lshl_add_u64 v[142:143], v[140:141], 0, s[30:31]
	global_load_dwordx4 v[112:115], v[142:143], off nt
	v_lshl_add_u64 v[142:143], v[140:141], 0, s[32:33]
	global_load_dwordx4 v[116:119], v[142:143], off nt
	v_lshl_add_u64 v[142:143], v[140:141], 0, s[34:35]
	global_load_dwordx4 v[120:123], v[142:143], off nt
	s_add_u32 s4, s4, 0x60000
	s_addc_u32 s5, s5, 0
	ds_read_b128 v[132:135], v13
	ds_read_b128 v[136:139], v13 offset:16
	v_add_u32_e32 v13, 32, v13
	s_waitcnt vmcnt(15) lgkmcnt(2)
	v_fma_f32 v2, v60, v124, v2
	v_fma_f32 v3, v61, v124, v3
	v_fma_f32 v4, v62, v124, v4
	v_fma_f32 v5, v63, v124, v5
	s_waitcnt vmcnt(14)
	v_fma_f32 v2, v64, v125, v2
	v_fma_f32 v3, v65, v125, v3
	v_fma_f32 v4, v66, v125, v4
	v_fma_f32 v5, v67, v125, v5
	s_waitcnt vmcnt(13)
	v_fma_f32 v2, v68, v126, v2
	v_fma_f32 v3, v69, v126, v3
	v_fma_f32 v4, v70, v126, v4
	v_fma_f32 v5, v71, v126, v5
	s_waitcnt vmcnt(12)
	v_fma_f32 v2, v72, v127, v2
	v_fma_f32 v3, v73, v127, v3
	v_fma_f32 v4, v74, v127, v4
	v_fma_f32 v5, v75, v127, v5
	s_waitcnt vmcnt(11)
	v_fma_f32 v2, v76, v128, v2
	v_fma_f32 v3, v77, v128, v3
	v_fma_f32 v4, v78, v128, v4
	v_fma_f32 v5, v79, v128, v5
	s_waitcnt vmcnt(10)
	v_fma_f32 v2, v80, v129, v2
	v_fma_f32 v3, v81, v129, v3
	v_fma_f32 v4, v82, v129, v4
	v_fma_f32 v5, v83, v129, v5
	s_waitcnt vmcnt(9)
	v_fma_f32 v2, v84, v130, v2
	v_fma_f32 v3, v85, v130, v3
	v_fma_f32 v4, v86, v130, v4
	v_fma_f32 v5, v87, v130, v5
	s_waitcnt vmcnt(8)
	v_fma_f32 v2, v88, v131, v2
	v_fma_f32 v3, v89, v131, v3
	v_fma_f32 v4, v90, v131, v4
	v_fma_f32 v5, v91, v131, v5
	v_lshl_add_u64 v[140:141], v[10:11], 0, s[4:5]
	global_load_dwordx4 v[60:63], v[140:141], off nt
	v_lshl_add_u64 v[142:143], v[140:141], 0, s[22:23]
	global_load_dwordx4 v[64:67], v[142:143], off nt
	v_lshl_add_u64 v[142:143], v[140:141], 0, s[24:25]
	global_load_dwordx4 v[68:71], v[142:143], off nt
	v_lshl_add_u64 v[142:143], v[140:141], 0, s[26:27]
	global_load_dwordx4 v[72:75], v[142:143], off nt
	v_lshl_add_u64 v[142:143], v[140:141], 0, s[28:29]
	global_load_dwordx4 v[76:79], v[142:143], off nt
	v_lshl_add_u64 v[142:143], v[140:141], 0, s[30:31]
	global_load_dwordx4 v[80:83], v[142:143], off nt
	v_lshl_add_u64 v[142:143], v[140:141], 0, s[32:33]
	global_load_dwordx4 v[84:87], v[142:143], off nt
	v_lshl_add_u64 v[142:143], v[140:141], 0, s[34:35]
	global_load_dwordx4 v[88:91], v[142:143], off nt
	s_add_u32 s4, s4, 0x60000
	s_addc_u32 s5, s5, 0
	ds_read_b128 v[124:127], v13
	ds_read_b128 v[128:131], v13 offset:16
	v_add_u32_e32 v13, 32, v13
	s_waitcnt vmcnt(15) lgkmcnt(2)
	v_fma_f32 v2, v92, v132, v2
	v_fma_f32 v3, v93, v132, v3
	v_fma_f32 v4, v94, v132, v4
	v_fma_f32 v5, v95, v132, v5
	s_waitcnt vmcnt(14)
	v_fma_f32 v2, v96, v133, v2
	v_fma_f32 v3, v97, v133, v3
	v_fma_f32 v4, v98, v133, v4
	v_fma_f32 v5, v99, v133, v5
	s_waitcnt vmcnt(13)
	v_fma_f32 v2, v100, v134, v2
	v_fma_f32 v3, v101, v134, v3
	v_fma_f32 v4, v102, v134, v4
	v_fma_f32 v5, v103, v134, v5
	s_waitcnt vmcnt(12)
	v_fma_f32 v2, v104, v135, v2
	v_fma_f32 v3, v105, v135, v3
	v_fma_f32 v4, v106, v135, v4
	v_fma_f32 v5, v107, v135, v5
	s_waitcnt vmcnt(11)
	v_fma_f32 v2, v108, v136, v2
	v_fma_f32 v3, v109, v136, v3
	v_fma_f32 v4, v110, v136, v4
	v_fma_f32 v5, v111, v136, v5
	s_waitcnt vmcnt(10)
	v_fma_f32 v2, v112, v137, v2
	v_fma_f32 v3, v113, v137, v3
	v_fma_f32 v4, v114, v137, v4
	v_fma_f32 v5, v115, v137, v5
	s_waitcnt vmcnt(9)
	v_fma_f32 v2, v116, v138, v2
	v_fma_f32 v3, v117, v138, v3
	v_fma_f32 v4, v118, v138, v4
	v_fma_f32 v5, v119, v138, v5
	s_waitcnt vmcnt(8)
	v_fma_f32 v2, v120, v139, v2
	v_fma_f32 v3, v121, v139, v3
	v_fma_f32 v4, v122, v139, v4
	v_fma_f32 v5, v123, v139, v5
	s_add_u32 s36, s36, 1
	s_cmp_lg_u32 s36, 7
	s_cbranch_scc1 .Lada_loop
; #define LAS __attribute__((address_space(3)))
; __device__ __forceinline__ void ada_phase(LAS float* sm, int bid, int G, const float* c, const float* ada_w, const float* ada_b, float* ada) {
;     ...
;     for (int j = bid; j < 192; j += G) {
;         const int l = j / 96, cb = j - l * 96;
;         const float* w = ada_w + (size_t)l * D * 12288 + (size_t)(kg * 128) * 12288 + cb * 128 + c4 * 4;
;         float4 a = make_float4(0.f, 0.f, 0.f, 0.f);
; #pragma unroll 8
;         for (int k = 0; k < 128; ++k) { const float4 wv = *(const float4*)(w + (size_t)k * 12288); const float s = cs[kg * 128 + k]; a.x += s * wv.x; a.y += s * wv.y; a.z += s * wv.z; a.w += s * wv.w; }
;         __syncthreads();
;         LAS float* rp = red + kg * 128 + c4 * 4; rp[0] = a.x; rp[1] = a.y; rp[2] = a.z; rp[3] = a.w;
;         __syncthreads();
;         if (tid < 128) { float s = 0.f;
; #pragma unroll
;             for (int q = 0; q < 16; ++q) s += red[q * 128 + tid];
;             ada[l * 12288 + cb * 128 + tid] = s + ada_b[l * 12288 + cb * 128 + tid]; }
	v_lshl_add_u64 v[140:141], v[10:11], 0, s[4:5]
	global_load_dwordx4 v[92:95], v[140:141], off nt
	v_lshl_add_u64 v[142:143], v[140:141], 0, s[22:23]
	global_load_dwordx4 v[96:99], v[142:143], off nt
	v_lshl_add_u64 v[142:143], v[140:141], 0, s[24:25]
	global_load_dwordx4 v[100:103], v[142:143], off nt
	v_lshl_add_u64 v[142:143], v[140:141], 0, s[26:27]
	global_load_dwordx4 v[104:107], v[142:143], off nt
	v_lshl_add_u64 v[142:143], v[140:141], 0, s[28:29]
	global_load_dwordx4 v[108:111], v[142:143], off nt
	v_lshl_add_u64 v[142:143], v[140:141], 0, s[30:31]
	global_load_dwordx4 v[112:115], v[142:143], off nt
	v_lshl_add_u64 v[142:143], v[140:141], 0, s[32:33]
	global_load_dwordx4 v[116:119], v[142:143], off nt
	v_lshl_add_u64 v[142:143], v[140:141], 0, s[34:35]
	global_load_dwordx4 v[120:123], v[142:143], off nt
	s_add_u32 s4, s4, 0x60000
	s_addc_u32 s5, s5, 0
	ds_read_b128 v[132:135], v13
	ds_read_b128 v[136:139], v13 offset:16
	v_add_u32_e32 v13, 32, v13
	s_waitcnt vmcnt(15) lgkmcnt(2)
	v_fma_f32 v2, v60, v124, v2
	v_fma_f32 v3, v61, v124, v3
	v_fma_f32 v4, v62, v124, v4
	v_fma_f32 v5, v63, v124, v5
	s_waitcnt vmcnt(14)
	v_fma_f32 v2, v64, v125, v2
	v_fma_f32 v3, v65, v125, v3
	v_fma_f32 v4, v66, v125, v4
	v_fma_f32 v5, v67, v125, v5
	s_waitcnt vmcnt(13)
	v_fma_f32 v2, v68, v126, v2
	v_fma_f32 v3, v69, v126, v3
	v_fma_f32 v4, v70, v126, v4
	v_fma_f32 v5, v71, v126, v5
	s_waitcnt vmcnt(12)
	v_fma_f32 v2, v72, v127, v2
	v_fma_f32 v3, v73, v127, v3
	v_fma_f32 v4, v74, v127, v4
	v_fma_f32 v5, v75, v127, v5
	s_waitcnt vmcnt(11)
	v_fma_f32 v2, v76, v128, v2
	v_fma_f32 v3, v77, v128, v3
	v_fma_f32 v4, v78, v128, v4
	v_fma_f32 v5, v79, v128, v5
	s_waitcnt vmcnt(10)
	v_fma_f32 v2, v80, v129, v2
	v_fma_f32 v3, v81, v129, v3
	v_fma_f32 v4, v82, v129, v4
	v_fma_f32 v5, v83, v129, v5
	s_waitcnt vmcnt(9)
	v_fma_f32 v2, v84, v130, v2
	v_fma_f32 v3, v85, v130, v3
	v_fma_f32 v4, v86, v130, v4
	v_fma_f32 v5, v87, v130, v5
	s_waitcnt vmcnt(8)
	v_fma_f32 v2, v88, v131, v2
	v_fma_f32 v3, v89, v131, v3
	v_fma_f32 v4, v90, v131, v4
	v_fma_f32 v5, v91, v131, v5
	s_waitcnt vmcnt(7) lgkmcnt(0)
	v_fma_f32 v2, v92, v132, v2
	v_fma_f32 v3, v93, v132, v3
	v_fma_f32 v4, v94, v132, v4
	v_fma_f32 v5, v95, v132, v5
	s_waitcnt vmcnt(6)
	v_fma_f32 v2, v96, v133, v2
	v_fma_f32 v3, v97, v133, v3
	v_fma_f32 v4, v98, v133, v4
	v_fma_f32 v5, v99, v133, v5
	s_waitcnt vmcnt(5)
	v_fma_f32 v2, v100, v134, v2
	v_fma_f32 v3, v101, v134, v3
	v_fma_f32 v4, v102, v134, v4
	v_fma_f32 v5, v103, v134, v5
	s_waitcnt vmcnt(4)
	v_fma_f32 v2, v104, v135, v2
	v_fma_f32 v3, v105, v135, v3
	v_fma_f32 v4, v106, v135, v4
	v_fma_f32 v5, v107, v135, v5
	s_waitcnt vmcnt(3)
	v_fma_f32 v2, v108, v136, v2
	v_fma_f32 v3, v109, v136, v3
	v_fma_f32 v4, v110, v136, v4
	v_fma_f32 v5, v111, v136, v5
	s_waitcnt vmcnt(2)
	v_fma_f32 v2, v112, v137, v2
	v_fma_f32 v3, v113, v137, v3
	v_fma_f32 v4, v114, v137, v4
	v_fma_f32 v5, v115, v137, v5
	s_waitcnt vmcnt(1)
	v_fma_f32 v2, v116, v138, v2
	v_fma_f32 v3, v117, v138, v3
	v_fma_f32 v4, v118, v138, v4
	v_fma_f32 v5, v119, v138, v5
	s_waitcnt vmcnt(0)
	v_fma_f32 v2, v120, v139, v2
	v_fma_f32 v3, v121, v139, v3
	v_fma_f32 v4, v122, v139, v4
	v_fma_f32 v5, v123, v139, v5
	s_barrier
	ds_write_b128 v7, v[2:5] offset:8192
	s_waitcnt lgkmcnt(0)
	s_barrier
	s_and_saveexec_b64 s[4:5], s[0:1]
	s_cbranch_execz .LBB0_21
	s_mulk_i32 s19, 0xffa0
	s_add_i32 s19, s19, s17
	s_lshl_b32 s19, s19, 7
	s_add_i32 s19, s19, s18
	v_add_u32_e32 v2, s19, v6
	v_ashrrev_i32_e32 v3, 31, v2
	v_lshlrev_b64 v[2:3], 2, v[2:3]
	v_lshl_add_u64 v[4:5], s[6:7], 0, v[2:3]
	global_load_dword v13, v[4:5], off
	ds_read2st64_b32 v[4:5], v12 offset0:32 offset1:34
	ds_read2st64_b32 v[10:11], v12 offset0:36 offset1:38
	ds_read2st64_b32 v[14:15], v12 offset0:40 offset1:42
	ds_read2st64_b32 v[16:17], v12 offset0:44 offset1:46
	ds_read2st64_b32 v[18:19], v12 offset0:48 offset1:50
	ds_read2st64_b32 v[20:21], v12 offset0:52 offset1:54
	ds_read2st64_b32 v[22:23], v12 offset0:56 offset1:58
	ds_read2st64_b32 v[24:25], v12 offset0:60 offset1:62
	s_waitcnt lgkmcnt(7)
	v_add_f32_e32 v4, 0, v4
	v_add_f32_e32 v4, v4, v5
	s_waitcnt lgkmcnt(6)
	v_add_f32_e32 v4, v4, v10
	v_add_f32_e32 v4, v4, v11
	s_waitcnt lgkmcnt(5)
	v_add_f32_e32 v4, v4, v14
	v_add_f32_e32 v4, v4, v15
	s_waitcnt lgkmcnt(4)
	v_add_f32_e32 v4, v4, v16
	v_add_f32_e32 v4, v4, v17
	s_waitcnt lgkmcnt(3)
	v_add_f32_e32 v4, v4, v18
	v_add_f32_e32 v4, v4, v19
	s_waitcnt lgkmcnt(2)
	v_add_f32_e32 v4, v4, v20
	v_add_f32_e32 v4, v4, v21
	s_waitcnt lgkmcnt(1)
	v_add_f32_e32 v4, v4, v22
	v_add_f32_e32 v4, v4, v23
	s_waitcnt lgkmcnt(0)
	v_add_f32_e32 v4, v4, v24
	v_add_f32_e32 v4, v4, v25
	v_lshl_add_u64 v[2:3], s[2:3], 0, v[2:3]
	s_waitcnt vmcnt(0)
	v_add_f32_e32 v4, v4, v13
	global_store_dword v[2:3], v4, off
	s_branch .LBB0_21
